# v10 plus DSA fast path: v_pk_mul_f32 beside MFMAs split into two v_mul_f32 each
# baseline (speedup 1.0000x reference)
.Lmy_dsa_fast:
	v_addc_co_u32_e32 v45, vcc, 0, v45, vcc
	global_load_dwordx4 v[44:47], v[44:45], off
	s_nop 0
	global_load_dwordx4 v[138:141], v[134:135], off offset:64
	s_waitcnt vmcnt(1)
	v_cndmask_b32_e64 v137, v47, 0, s[38:39]
	v_cndmask_b32_e64 v136, v46, 0, s[38:39]
	v_cndmask_b32_e64 v135, v45, 0, s[38:39]
	v_cndmask_b32_e64 v134, v44, 0, s[38:39]
	s_waitcnt vmcnt(0)
	v_cndmask_b32_e64 v47, v141, 0, s[38:39]
	v_cndmask_b32_e64 v46, v140, 0, s[38:39]
	v_cndmask_b32_e64 v45, v139, 0, s[38:39]
	v_cndmask_b32_e64 v44, v138, 0, s[38:39]
	ds_bpermute_b32 v102, v248, v0
	ds_bpermute_b32 v103, v248, v1
	ds_bpermute_b32 v104, v248, v2
	ds_bpermute_b32 v105, v248, v3
	ds_bpermute_b32 v106, v248, v4
	ds_bpermute_b32 v107, v248, v5
	ds_bpermute_b32 v108, v248, v6
	ds_bpermute_b32 v109, v248, v7
	ds_bpermute_b32 v110, v248, v8
	ds_bpermute_b32 v111, v248, v9
	ds_bpermute_b32 v112, v248, v10
	ds_bpermute_b32 v113, v248, v11
	ds_bpermute_b32 v114, v248, v12
	ds_bpermute_b32 v115, v248, v13
	ds_bpermute_b32 v116, v248, v14
	ds_bpermute_b32 v117, v248, v15
	s_waitcnt lgkmcnt(12)
	v_mfma_f32_16x16x32_bf16 v[140:143], v[102:105], v[134:137], 0
	s_waitcnt lgkmcnt(8)
	v_mfma_f32_16x16x32_bf16 v[142:145], v[106:109], v[44:47], v[140:143]
	ds_bpermute_b32 v102, v248, v16
	ds_bpermute_b32 v103, v248, v17
	ds_bpermute_b32 v104, v248, v18
	ds_bpermute_b32 v105, v248, v19
	ds_bpermute_b32 v106, v248, v20
	ds_bpermute_b32 v107, v248, v21
	ds_bpermute_b32 v108, v248, v22
	ds_bpermute_b32 v109, v248, v23
	s_nop 1
	v_mul_f32_e32 v142, s74, v142
	v_mul_f32_e32 v143, s74, v143
	v_mul_f32_e32 v140, s74, v144
	v_mul_f32_e32 v141, s74, v145
	v_max3_f32 v49, v142, s82, v143
	v_max3_f32 v49, v49, v140, v141
	s_waitcnt lgkmcnt(12)
	v_mfma_f32_16x16x32_bf16 v[154:157], v[110:113], v[134:137], 0
	s_waitcnt lgkmcnt(8)
	v_mfma_f32_16x16x32_bf16 v[154:157], v[114:117], v[44:47], v[154:157]
	ds_bpermute_b32 v110, v248, v24
	ds_bpermute_b32 v111, v248, v25
	ds_bpermute_b32 v112, v248, v26
	ds_bpermute_b32 v113, v248, v27
	ds_bpermute_b32 v114, v248, v28
	ds_bpermute_b32 v115, v248, v29
	ds_bpermute_b32 v116, v248, v30
	ds_bpermute_b32 v117, v248, v31
	s_nop 1
	v_mul_f32_e32 v144, s74, v154
	v_mul_f32_e32 v145, s74, v155
	v_mul_f32_e32 v138, s74, v156
	v_mul_f32_e32 v139, s74, v157
	v_max3_f32 v49, v49, v144, v145
	v_max3_f32 v49, v49, v138, v139
	s_waitcnt lgkmcnt(12)
	v_mfma_f32_16x16x32_bf16 v[156:159], v[102:105], v[134:137], 0
	s_waitcnt lgkmcnt(8)
	v_mfma_f32_16x16x32_bf16 v[158:161], v[106:109], v[44:47], v[156:159]
	ds_bpermute_b32 v102, v248, v32
	ds_bpermute_b32 v103, v248, v33
	ds_bpermute_b32 v104, v248, v34
	ds_bpermute_b32 v105, v248, v35
	ds_bpermute_b32 v106, v248, v36
	ds_bpermute_b32 v107, v248, v37
	ds_bpermute_b32 v108, v248, v38
	ds_bpermute_b32 v109, v248, v39
	s_nop 1
	v_mul_f32_e32 v158, s74, v158
	v_mul_f32_e32 v159, s74, v159
	v_mul_f32_e32 v156, s74, v160
	v_mul_f32_e32 v157, s74, v161
	v_max3_f32 v49, v49, v158, v159
	v_max3_f32 v49, v49, v156, v157
	s_waitcnt lgkmcnt(12)
	v_mfma_f32_16x16x32_bf16 v[160:163], v[110:113], v[134:137], 0
	s_waitcnt lgkmcnt(8)
	v_mfma_f32_16x16x32_bf16 v[160:163], v[114:117], v[44:47], v[160:163]
	ds_bpermute_b32 v110, v248, v40
	ds_bpermute_b32 v111, v248, v41
	ds_bpermute_b32 v112, v248, v42
	ds_bpermute_b32 v113, v248, v43
	ds_bpermute_b32 v114, v248, v50
	ds_bpermute_b32 v115, v248, v51
	ds_bpermute_b32 v116, v248, v52
	ds_bpermute_b32 v117, v248, v53
	s_nop 1
	v_mul_f32_e32 v160, s74, v160
	v_mul_f32_e32 v161, s74, v161
	v_mul_f32_e32 v154, s74, v162
	v_mul_f32_e32 v155, s74, v163
	v_max3_f32 v49, v49, v160, v161
	v_max3_f32 v49, v49, v154, v155
	s_waitcnt lgkmcnt(12)
	v_mfma_f32_16x16x32_bf16 v[164:167], v[102:105], v[134:137], 0
	s_waitcnt lgkmcnt(8)
	v_mfma_f32_16x16x32_bf16 v[166:169], v[106:109], v[44:47], v[164:167]
	ds_bpermute_b32 v102, v248, v54
	ds_bpermute_b32 v103, v248, v55
	ds_bpermute_b32 v104, v248, v56
	ds_bpermute_b32 v105, v248, v57
	ds_bpermute_b32 v106, v248, v58
	ds_bpermute_b32 v107, v248, v59
	ds_bpermute_b32 v108, v248, v60
	ds_bpermute_b32 v109, v248, v61
	s_nop 1
	v_mul_f32_e32 v166, s74, v166
	v_mul_f32_e32 v167, s74, v167
	v_mul_f32_e32 v164, s74, v168
	v_mul_f32_e32 v165, s74, v169
	v_max3_f32 v49, v49, v166, v167
	v_max3_f32 v49, v49, v164, v165
	s_waitcnt lgkmcnt(12)
	v_mfma_f32_16x16x32_bf16 v[168:171], v[110:113], v[134:137], 0
	s_waitcnt lgkmcnt(8)
	v_mfma_f32_16x16x32_bf16 v[168:171], v[114:117], v[44:47], v[168:171]
	ds_bpermute_b32 v110, v248, v62
	ds_bpermute_b32 v111, v248, v63
	ds_bpermute_b32 v112, v248, v64
	ds_bpermute_b32 v113, v248, v65
	ds_bpermute_b32 v114, v248, v66
	ds_bpermute_b32 v115, v248, v67
	ds_bpermute_b32 v116, v248, v68
	ds_bpermute_b32 v117, v248, v69
	s_nop 1
	v_mul_f32_e32 v168, s74, v168
	v_mul_f32_e32 v169, s74, v169
	v_mul_f32_e32 v162, s74, v170
	v_mul_f32_e32 v163, s74, v171
	v_max3_f32 v49, v49, v168, v169
	v_max3_f32 v49, v49, v162, v163
	s_waitcnt lgkmcnt(12)
	v_mfma_f32_16x16x32_bf16 v[172:175], v[102:105], v[134:137], 0
	s_waitcnt lgkmcnt(8)
	v_mfma_f32_16x16x32_bf16 v[174:177], v[106:109], v[44:47], v[172:175]
	s_nop 7
	v_mul_f32_e32 v174, s74, v174
	v_mul_f32_e32 v175, s74, v175
	v_mul_f32_e32 v172, s74, v176
	v_mul_f32_e32 v173, s74, v177
	v_max3_f32 v49, v49, v174, v175
	v_max3_f32 v49, v49, v172, v173
	s_waitcnt lgkmcnt(4)
	v_mfma_f32_16x16x32_bf16 v[176:179], v[110:113], v[134:137], 0
	s_waitcnt lgkmcnt(0)
	v_mfma_f32_16x16x32_bf16 v[176:179], v[114:117], v[44:47], v[176:179]
	s_nop 7
	v_mul_f32_e32 v176, s74, v176
	v_mul_f32_e32 v177, s74, v177
	v_mul_f32_e32 v170, s74, v178
	v_mul_f32_e32 v171, s74, v179
	v_max3_f32 v49, v49, v176, v177
	v_max3_f32 v49, v49, v170, v171
	s_lshl_b32 s6, s6, 9
	s_add_i32 s19, s6, 0
	s_add_i32 s19, s19, 0x20000
	v_lshl_add_u32 v151, v147, 1, s19
	ds_read_u16 v0, v151 offset:256
	ds_read_u16 v8, v151 offset:288
	ds_read_u16 v16, v151 offset:320
	ds_read_u16 v24, v151 offset:352
	ds_read_u16 v32, v151 offset:384
	ds_read_u16 v40, v151 offset:416
	ds_read_u16 v54, v151 offset:448
	ds_read_u16 v62, v151 offset:480
	s_waitcnt lgkmcnt(0)
	v_lshl_or_b32 v4, v0, 8, v246
	global_load_dwordx4 v[0:3], v4, s[50:51]
	global_load_dwordx4 v[4:7], v4, s[50:51] offset:64
	v_lshl_or_b32 v12, v8, 8, v246
	global_load_dwordx4 v[8:11], v12, s[50:51]
	global_load_dwordx4 v[12:15], v12, s[50:51] offset:64
	v_lshl_or_b32 v20, v16, 8, v246
	global_load_dwordx4 v[16:19], v20, s[50:51]
	global_load_dwordx4 v[20:23], v20, s[50:51] offset:64
	v_lshl_or_b32 v28, v24, 8, v246
	global_load_dwordx4 v[24:27], v28, s[50:51]
	global_load_dwordx4 v[28:31], v28, s[50:51] offset:64
	v_lshl_or_b32 v36, v32, 8, v246
	global_load_dwordx4 v[32:35], v36, s[50:51]
	global_load_dwordx4 v[36:39], v36, s[50:51] offset:64
	v_lshl_or_b32 v50, v40, 8, v246
	global_load_dwordx4 v[40:43], v50, s[50:51]
	global_load_dwordx4 v[50:53], v50, s[50:51] offset:64
	v_lshl_or_b32 v58, v54, 8, v246
	global_load_dwordx4 v[54:57], v58, s[50:51]
	global_load_dwordx4 v[58:61], v58, s[50:51] offset:64
	v_lshl_or_b32 v66, v62, 8, v246
	global_load_dwordx4 v[62:65], v66, s[50:51]
	global_load_dwordx4 v[66:69], v66, s[50:51] offset:64
	s_xor_b64 s[6:7], s[44:45], -1
	s_ashr_i32 s53, s52, 31
	s_waitcnt vmcnt(15)
	ds_bpermute_b32 v102, v248, v0
	ds_bpermute_b32 v103, v248, v1
	ds_bpermute_b32 v104, v248, v2
	ds_bpermute_b32 v105, v248, v3
	s_waitcnt vmcnt(14)
	ds_bpermute_b32 v106, v248, v4
	ds_bpermute_b32 v107, v248, v5
	ds_bpermute_b32 v108, v248, v6
	ds_bpermute_b32 v109, v248, v7
	s_waitcnt vmcnt(13)
	ds_bpermute_b32 v110, v248, v8
	ds_bpermute_b32 v111, v248, v9
	ds_bpermute_b32 v112, v248, v10
	ds_bpermute_b32 v113, v248, v11
	s_waitcnt vmcnt(12)
	ds_bpermute_b32 v114, v248, v12
	ds_bpermute_b32 v115, v248, v13
	ds_bpermute_b32 v116, v248, v14
	ds_bpermute_b32 v117, v248, v15
	s_waitcnt lgkmcnt(12)
	v_mfma_f32_16x16x32_bf16 v[180:183], v[102:105], v[134:137], 0
	s_waitcnt lgkmcnt(8)
	v_mfma_f32_16x16x32_bf16 v[182:185], v[106:109], v[44:47], v[180:183]
	s_waitcnt vmcnt(11)
	ds_bpermute_b32 v102, v248, v16
	ds_bpermute_b32 v103, v248, v17
	ds_bpermute_b32 v104, v248, v18
	ds_bpermute_b32 v105, v248, v19
	s_waitcnt vmcnt(10)
	ds_bpermute_b32 v106, v248, v20
	ds_bpermute_b32 v107, v248, v21
	ds_bpermute_b32 v108, v248, v22
	ds_bpermute_b32 v109, v248, v23
	s_nop 1
	v_mul_f32_e32 v182, s74, v182
	v_mul_f32_e32 v183, s74, v183
	v_mul_f32_e32 v180, s74, v184
	v_mul_f32_e32 v181, s74, v185
	v_max3_f32 v49, v49, v182, v183
	v_max3_f32 v49, v49, v180, v181
	s_waitcnt lgkmcnt(12)
	v_mfma_f32_16x16x32_bf16 v[184:187], v[110:113], v[134:137], 0
	s_waitcnt lgkmcnt(8)
	v_mfma_f32_16x16x32_bf16 v[184:187], v[114:117], v[44:47], v[184:187]
	s_waitcnt vmcnt(9)
	ds_bpermute_b32 v110, v248, v24
	ds_bpermute_b32 v111, v248, v25
	ds_bpermute_b32 v112, v248, v26
	ds_bpermute_b32 v113, v248, v27
	s_waitcnt vmcnt(8)
	ds_bpermute_b32 v114, v248, v28
	ds_bpermute_b32 v115, v248, v29
	ds_bpermute_b32 v116, v248, v30
	ds_bpermute_b32 v117, v248, v31
	s_nop 1
	v_mul_f32_e32 v184, s74, v184
	v_mul_f32_e32 v185, s74, v185
	v_mul_f32_e32 v178, s74, v186
	v_mul_f32_e32 v179, s74, v187
	v_max3_f32 v49, v49, v184, v185
	v_max3_f32 v49, v49, v178, v179
	s_waitcnt lgkmcnt(12)
	v_mfma_f32_16x16x32_bf16 v[188:191], v[102:105], v[134:137], 0
	s_waitcnt lgkmcnt(8)
	v_mfma_f32_16x16x32_bf16 v[190:193], v[106:109], v[44:47], v[188:191]
	s_waitcnt vmcnt(7)
	ds_bpermute_b32 v102, v248, v32
	ds_bpermute_b32 v103, v248, v33
	ds_bpermute_b32 v104, v248, v34
	ds_bpermute_b32 v105, v248, v35
	s_waitcnt vmcnt(6)
	ds_bpermute_b32 v106, v248, v36
	ds_bpermute_b32 v107, v248, v37
	ds_bpermute_b32 v108, v248, v38
	ds_bpermute_b32 v109, v248, v39
	s_nop 1
	v_mul_f32_e32 v190, s74, v190
	v_mul_f32_e32 v191, s74, v191
	v_mul_f32_e32 v188, s74, v192
	v_mul_f32_e32 v189, s74, v193
	v_max3_f32 v49, v49, v190, v191
	v_max3_f32 v49, v49, v188, v189
	s_waitcnt lgkmcnt(12)
	v_mfma_f32_16x16x32_bf16 v[192:195], v[110:113], v[134:137], 0
	s_waitcnt lgkmcnt(8)
	v_mfma_f32_16x16x32_bf16 v[192:195], v[114:117], v[44:47], v[192:195]
	s_waitcnt vmcnt(5)
	ds_bpermute_b32 v110, v248, v40
	ds_bpermute_b32 v111, v248, v41
	ds_bpermute_b32 v112, v248, v42
	ds_bpermute_b32 v113, v248, v43
	s_waitcnt vmcnt(4)
	ds_bpermute_b32 v114, v248, v50
	ds_bpermute_b32 v115, v248, v51
	ds_bpermute_b32 v116, v248, v52
	ds_bpermute_b32 v117, v248, v53
	s_nop 1
	v_mul_f32_e32 v192, s74, v192
	v_mul_f32_e32 v193, s74, v193
	v_mul_f32_e32 v186, s74, v194
	v_mul_f32_e32 v187, s74, v195
	v_max3_f32 v49, v49, v192, v193
	v_max3_f32 v49, v49, v186, v187
	s_waitcnt lgkmcnt(12)
	v_mfma_f32_16x16x32_bf16 v[196:199], v[102:105], v[134:137], 0
	s_waitcnt lgkmcnt(8)
	v_mfma_f32_16x16x32_bf16 v[196:199], v[106:109], v[44:47], v[196:199]
	s_waitcnt vmcnt(3)
	ds_bpermute_b32 v102, v248, v54
	ds_bpermute_b32 v103, v248, v55
	ds_bpermute_b32 v104, v248, v56
	ds_bpermute_b32 v105, v248, v57
	s_waitcnt vmcnt(2)
	ds_bpermute_b32 v106, v248, v58
	ds_bpermute_b32 v107, v248, v59
	ds_bpermute_b32 v108, v248, v60
	ds_bpermute_b32 v109, v248, v61
	s_nop 1
	v_mul_f32_e32 v200, s74, v196
	v_mul_f32_e32 v201, s74, v197
	v_mul_f32_e32 v198, s74, v198
	v_mul_f32_e32 v199, s74, v199
	v_max3_f32 v49, v49, v200, v201
	v_max3_f32 v49, v49, v198, v199
	s_waitcnt lgkmcnt(12)
	v_mfma_f32_16x16x32_bf16 v[194:197], v[110:113], v[134:137], 0
	s_waitcnt lgkmcnt(8)
	v_mfma_f32_16x16x32_bf16 v[194:197], v[114:117], v[44:47], v[194:197]
	s_waitcnt vmcnt(1)
	ds_bpermute_b32 v110, v248, v62
	ds_bpermute_b32 v111, v248, v63
	ds_bpermute_b32 v112, v248, v64
	ds_bpermute_b32 v113, v248, v65
	s_waitcnt vmcnt(0)
	ds_bpermute_b32 v114, v248, v66
	ds_bpermute_b32 v115, v248, v67
	ds_bpermute_b32 v116, v248, v68
	ds_bpermute_b32 v117, v248, v69
	s_nop 1
	v_mul_f32_e32 v202, s74, v194
	v_mul_f32_e32 v203, s74, v195
	v_mul_f32_e32 v194, s74, v196
	v_mul_f32_e32 v195, s74, v197
	v_max3_f32 v49, v49, v202, v203
	v_max3_f32 v49, v49, v194, v195
	s_waitcnt lgkmcnt(12)
	v_mfma_f32_16x16x32_bf16 v[206:209], v[102:105], v[134:137], 0
	s_waitcnt lgkmcnt(8)
	v_mfma_f32_16x16x32_bf16 v[206:209], v[106:109], v[44:47], v[206:209]
	s_nop 7
	v_mul_f32_e32 v212, s74, v206
	v_mul_f32_e32 v213, s74, v207
	v_mul_f32_e32 v210, s74, v208
	v_mul_f32_e32 v211, s74, v209
	v_max3_f32 v49, v49, v212, v213
	v_max3_f32 v49, v49, v210, v211
	s_waitcnt lgkmcnt(4)
	v_mfma_f32_16x16x32_bf16 v[134:137], v[110:113], v[134:137], 0
	s_waitcnt lgkmcnt(0)
	v_mfma_f32_16x16x32_bf16 v[44:47], v[114:117], v[44:47], v[134:137]
	s_nop 7
	v_mul_f32_e32 v44, s74, v44
	v_mul_f32_e32 v45, s74, v45
	s_nop 0
	v_max3_f32 v49, v49, v44, v45
	v_mul_f32_e32 v204, s74, v46
	v_mul_f32_e32 v205, s74, v47
	s_nop 0
	v_max3_f32 v49, v49, v204, v205
	s_and_b64 vcc, exec, s[44:45]
	s_cbranch_vccz .Lmy_dsa_fast_nk_skip
	ds_read_u16 v0, v251
	ds_read_u16 v8, v251 offset:32
	ds_read_u16 v16, v251 offset:64
	ds_read_u16 v24, v251 offset:96
	ds_read_u16 v32, v251 offset:128
	ds_read_u16 v40, v251 offset:160
	ds_read_u16 v54, v251 offset:192
	ds_read_u16 v62, v251 offset:224
	s_waitcnt lgkmcnt(0)
	v_lshl_or_b32 v4, v0, 8, v246
	global_load_dwordx4 v[0:3], v4, s[50:51]
	global_load_dwordx4 v[4:7], v4, s[50:51] offset:64
	v_lshl_or_b32 v12, v8, 8, v246
	global_load_dwordx4 v[8:11], v12, s[50:51]
	global_load_dwordx4 v[12:15], v12, s[50:51] offset:64
	v_lshl_or_b32 v20, v16, 8, v246
	global_load_dwordx4 v[16:19], v20, s[50:51]
	global_load_dwordx4 v[20:23], v20, s[50:51] offset:64
	v_lshl_or_b32 v28, v24, 8, v246
	global_load_dwordx4 v[24:27], v28, s[50:51]
	global_load_dwordx4 v[28:31], v28, s[50:51] offset:64
	v_lshl_or_b32 v36, v32, 8, v246
	global_load_dwordx4 v[32:35], v36, s[50:51]
	global_load_dwordx4 v[36:39], v36, s[50:51] offset:64
	v_lshl_or_b32 v50, v40, 8, v246
	global_load_dwordx4 v[40:43], v50, s[50:51]
	global_load_dwordx4 v[50:53], v50, s[50:51] offset:64
	v_lshl_or_b32 v58, v54, 8, v246
	global_load_dwordx4 v[54:57], v58, s[50:51]
	global_load_dwordx4 v[58:61], v58, s[50:51] offset:64
	v_lshl_or_b32 v66, v62, 8, v246
	global_load_dwordx4 v[62:65], v66, s[50:51]
	global_load_dwordx4 v[66:69], v66, s[50:51] offset:64
.Lmy_dsa_fast_nk_skip:
	v_lshl_add_u32 v151, v247, 1, s19
	ds_read_u16 v46, v151
	ds_read_u16 v47, v151 offset:16
	ds_read_u16 v126, v151 offset:32
	ds_read_u16 v127, v151 offset:48
	s_waitcnt lgkmcnt(0)
	v_lshl_or_b32 v46, v46, 8, v250
	v_lshl_or_b32 v47, v47, 8, v250
	global_load_dwordx4 v[102:105], v46, s[50:51] offset:128
	global_load_dwordx4 v[110:113], v47, s[50:51] offset:128
	v_lshl_or_b32 v46, v126, 8, v250
	v_lshl_or_b32 v47, v127, 8, v250
	global_load_dwordx4 v[126:129], v46, s[50:51] offset:128
	global_load_dwordx4 v[130:133], v47, s[50:51] offset:128
	ds_read_u16 v46, v151 offset:64
	ds_read_u16 v47, v151 offset:80
	ds_read_u16 v118, v151 offset:96
	ds_read_u16 v119, v151 offset:112
	s_waitcnt lgkmcnt(0)
	v_lshl_or_b32 v46, v46, 8, v250
	v_lshl_or_b32 v47, v47, 8, v250
	global_load_dwordx4 v[86:89], v46, s[50:51] offset:128
	global_load_dwordx4 v[94:97], v47, s[50:51] offset:128
	v_lshl_or_b32 v46, v118, 8, v250
	v_lshl_or_b32 v47, v119, 8, v250
	global_load_dwordx4 v[118:121], v46, s[50:51] offset:128
	global_load_dwordx4 v[122:125], v47, s[50:51] offset:128
	ds_read_u16 v46, v151 offset:128
	ds_read_u16 v47, v151 offset:144
	ds_read_u16 v106, v151 offset:160
	ds_read_u16 v107, v151 offset:176
	s_waitcnt lgkmcnt(0)
	v_lshl_or_b32 v46, v46, 8, v250
	v_lshl_or_b32 v47, v47, 8, v250
	global_load_dwordx4 v[78:81], v46, s[50:51] offset:128
	global_load_dwordx4 v[82:85], v47, s[50:51] offset:128
	v_lshl_or_b32 v46, v106, 8, v250
	v_lshl_or_b32 v47, v107, 8, v250
	global_load_dwordx4 v[106:109], v46, s[50:51] offset:128
	global_load_dwordx4 v[114:117], v47, s[50:51] offset:128
	ds_read_u16 v46, v151 offset:192
	ds_read_u16 v47, v151 offset:208
	ds_read_u16 v90, v151 offset:224
	ds_read_u16 v91, v151 offset:240
	s_waitcnt lgkmcnt(0)
	v_lshl_or_b32 v46, v46, 8, v250
	v_lshl_or_b32 v47, v47, 8, v250
	global_load_dwordx4 v[70:73], v46, s[50:51] offset:128
	global_load_dwordx4 v[74:77], v47, s[50:51] offset:128
	v_lshl_or_b32 v46, v90, 8, v250
	v_lshl_or_b32 v47, v91, 8, v250
	global_load_dwordx4 v[90:93], v46, s[50:51] offset:128
	global_load_dwordx4 v[98:101], v47, s[50:51] offset:128
	v_mov_b32_e32 v46, v49
	s_nop 1
	v_permlane32_swap_b32 v49, v46
	s_nop 1
	s_nop 0
	v_max_f32_e32 v46, v46, v46
	v_max_f32_e32 v47, v49, v49
	v_max_f32_e32 v46, v47, v46
	v_mov_b32_e32 v47, v46
	s_nop 1
	v_permlane16_swap_b32 v46, v47
	s_nop 1
	s_nop 0
	v_max_f32_e32 v47, v47, v47
	v_max_f32_e32 v46, v46, v46
	v_max_f32_e32 v49, v46, v47
	s_mov_b32 s32, 0x3fb8aa3b
	v_mul_f32_e32 v49, 0xbfb8aa3b, v49
	v_fma_f32 v135, v141, s32, v49
	v_fma_f32 v141, v158, s32, v49
	v_exp_f32_e32 v226, v141
	v_fma_f32 v141, v159, s32, v49
	v_exp_f32_e32 v227, v141
	v_fma_f32 v141, v156, s32, v49
	v_exp_f32_e32 v228, v141
	v_fma_f32 v141, v157, s32, v49
	v_exp_f32_e32 v229, v141
	v_fma_f32 v141, v160, s32, v49
	v_exp_f32_e32 v230, v141
	v_fma_f32 v141, v161, s32, v49
	v_exp_f32_e32 v231, v141
	v_fma_f32 v141, v154, s32, v49
	v_exp_f32_e32 v232, v141
	v_fma_f32 v141, v155, s32, v49
	v_exp_f32_e32 v233, v141
	v_fma_f32 v141, v166, s32, v49
	v_exp_f32_e32 v218, v141
	v_fma_f32 v141, v167, s32, v49
	v_exp_f32_e32 v219, v141
	v_fma_f32 v141, v164, s32, v49
	v_exp_f32_e32 v220, v141
	v_fma_f32 v141, v165, s32, v49
	v_exp_f32_e32 v221, v141
	v_fma_f32 v141, v168, s32, v49
	v_exp_f32_e32 v222, v141
	v_fma_f32 v141, v169, s32, v49
	v_exp_f32_e32 v223, v141
	v_fma_f32 v141, v162, s32, v49
	v_exp_f32_e32 v224, v141
	v_fma_f32 v141, v163, s32, v49
	v_exp_f32_e32 v225, v141
	v_fma_f32 v141, v174, s32, v49
	v_exp_f32_e32 v206, v141
	v_fma_f32 v141, v175, s32, v49
	v_exp_f32_e32 v207, v141
	v_fma_f32 v141, v172, s32, v49
	v_fma_f32 v46, v142, s32, v49
	v_exp_f32_e32 v208, v141
	v_fma_f32 v141, v173, s32, v49
	v_fma_f32 v47, v143, s32, v49
	v_exp_f32_e32 v46, v46
	v_fma_f32 v134, v140, s32, v49
	v_exp_f32_e32 v209, v141
	v_fma_f32 v141, v176, s32, v49
	v_exp_f32_e32 v47, v47
	v_exp_f32_e32 v134, v134
	v_exp_f32_e32 v214, v141
	v_fma_f32 v141, v177, s32, v49
	v_exp_f32_e32 v135, v135
	v_add_f32_e32 v136, 0, v46
	v_exp_f32_e32 v215, v141
	v_fma_f32 v141, v170, s32, v49
	v_add_f32_e32 v136, v47, v136
	v_add_f32_e32 v136, v134, v136
	v_exp_f32_e32 v216, v141
	v_fma_f32 v141, v171, s32, v49
	v_add_f32_e32 v140, v135, v136
	v_fma_f32 v136, v144, s32, v49
	v_fma_f32 v137, v145, s32, v49
	v_exp_f32_e32 v217, v141
	v_fma_f32 v141, v182, s32, v49
	v_exp_f32_e32 v136, v136
	v_fma_f32 v138, v138, s32, v49
	v_exp_f32_e32 v137, v137
	v_fma_f32 v139, v139, s32, v49
	v_exp_f32_e32 v182, v141
	v_fma_f32 v141, v183, s32, v49
	v_exp_f32_e32 v138, v138
	v_exp_f32_e32 v139, v139
	v_exp_f32_e32 v183, v141
	v_fma_f32 v141, v180, s32, v49
	v_add_f32_e32 v140, v136, v140
	v_add_f32_e32 v140, v137, v140
	v_exp_f32_e32 v180, v141
	v_fma_f32 v141, v181, s32, v49
	v_add_f32_e32 v140, v138, v140
	v_add_f32_e32 v140, v139, v140
	v_exp_f32_e32 v181, v141
	v_fma_f32 v141, v184, s32, v49
	v_add_f32_e32 v140, v226, v140
	v_add_f32_e32 v140, v227, v140
	v_exp_f32_e32 v184, v141
	v_fma_f32 v141, v185, s32, v49
	v_add_f32_e32 v140, v228, v140
	v_add_f32_e32 v140, v229, v140
	v_exp_f32_e32 v185, v141
	v_fma_f32 v141, v178, s32, v49
	v_add_f32_e32 v140, v230, v140
	v_add_f32_e32 v140, v231, v140
	v_exp_f32_e32 v196, v141
	v_fma_f32 v141, v179, s32, v49
	v_add_f32_e32 v140, v232, v140
	v_add_f32_e32 v140, v233, v140
	v_exp_f32_e32 v197, v141
	v_fma_f32 v141, v190, s32, v49
	v_add_f32_e32 v140, v218, v140
	v_add_f32_e32 v140, v219, v140
	v_exp_f32_e32 v172, v141
	v_fma_f32 v141, v191, s32, v49
	v_add_f32_e32 v140, v220, v140
	v_add_f32_e32 v140, v221, v140
	v_exp_f32_e32 v173, v141
	v_fma_f32 v141, v188, s32, v49
	v_add_f32_e32 v140, v222, v140
	v_add_f32_e32 v140, v223, v140
	v_exp_f32_e32 v174, v141
	v_fma_f32 v141, v189, s32, v49
	v_add_f32_e32 v140, v224, v140
	v_add_f32_e32 v140, v225, v140
	v_exp_f32_e32 v175, v141
	v_fma_f32 v141, v192, s32, v49
	v_add_f32_e32 v140, v206, v140
	v_add_f32_e32 v140, v207, v140
	v_exp_f32_e32 v176, v141
	v_fma_f32 v141, v193, s32, v49
	v_add_f32_e32 v140, v208, v140
	v_add_f32_e32 v140, v209, v140
	v_exp_f32_e32 v177, v141
	v_fma_f32 v141, v186, s32, v49
	v_add_f32_e32 v140, v214, v140
	v_add_f32_e32 v140, v215, v140
	v_exp_f32_e32 v178, v141
	v_fma_f32 v141, v187, s32, v49
	v_add_f32_e32 v140, v216, v140
	v_add_f32_e32 v140, v217, v140
	v_exp_f32_e32 v179, v141
	v_fma_f32 v141, v200, s32, v49
	v_add_f32_e32 v140, v182, v140
	v_add_f32_e32 v140, v183, v140
	v_exp_f32_e32 v164, v141
	v_fma_f32 v141, v201, s32, v49
	v_add_f32_e32 v140, v180, v140
	v_add_f32_e32 v140, v181, v140
	v_exp_f32_e32 v165, v141
	v_fma_f32 v141, v198, s32, v49
	v_add_f32_e32 v140, v184, v140
	v_add_f32_e32 v140, v185, v140
	v_exp_f32_e32 v166, v141
	v_fma_f32 v141, v199, s32, v49
	v_add_f32_e32 v140, v196, v140
	v_add_f32_e32 v140, v197, v140
	v_exp_f32_e32 v167, v141
	v_fma_f32 v141, v202, s32, v49
	v_add_f32_e32 v140, v172, v140
	v_add_f32_e32 v140, v173, v140
	v_exp_f32_e32 v168, v141
	v_fma_f32 v141, v203, s32, v49
	v_add_f32_e32 v140, v174, v140
	v_add_f32_e32 v140, v175, v140
	v_exp_f32_e32 v169, v141
	v_fma_f32 v141, v194, s32, v49
	v_add_f32_e32 v140, v176, v140
	v_add_f32_e32 v140, v177, v140
	v_exp_f32_e32 v170, v141
	v_fma_f32 v141, v195, s32, v49
	v_add_f32_e32 v140, v178, v140
	v_add_f32_e32 v140, v179, v140
	v_exp_f32_e32 v171, v141
	v_fma_f32 v141, v212, s32, v49
	v_add_f32_e32 v140, v164, v140
	v_add_f32_e32 v140, v165, v140
	v_exp_f32_e32 v154, v141
	v_fma_f32 v141, v213, s32, v49
	v_add_f32_e32 v140, v166, v140
	v_add_f32_e32 v140, v167, v140
	v_exp_f32_e32 v155, v141
	v_fma_f32 v141, v210, s32, v49
	v_fma_f32 v44, v44, s32, v49
	v_add_f32_e32 v140, v168, v140
	v_add_f32_e32 v140, v169, v140
	v_exp_f32_e32 v156, v141
	v_fma_f32 v141, v211, s32, v49
	v_exp_f32_e32 v158, v44
	v_fma_f32 v44, v45, s32, v49
	v_add_f32_e32 v140, v170, v140
	v_add_f32_e32 v140, v171, v140
	v_exp_f32_e32 v157, v141
	v_exp_f32_e32 v159, v44
	v_fma_f32 v44, v204, s32, v49
	v_add_f32_e32 v140, v154, v140
	v_add_f32_e32 v140, v155, v140
	v_exp_f32_e32 v160, v44
	v_fma_f32 v44, v205, s32, v49
	v_add_f32_e32 v140, v156, v140
	v_add_f32_e32 v140, v157, v140
	v_exp_f32_e32 v161, v44
	v_add_f32_e32 v44, v158, v140
	v_add_f32_e32 v44, v159, v44
	v_add_f32_e32 v44, v160, v44
	v_add_f32_e32 v44, v161, v44
	v_mov_b32_e32 v45, v44
	s_nop 1
	v_permlane32_swap_b32 v44, v45
	s_nop 1
	s_nop 0
	v_add_f32_e32 v44, v44, v45
	v_mov_b32_e32 v45, v44
	s_nop 1
	v_permlane16_swap_b32 v44, v45
	s_nop 1
	s_nop 0
	v_add_f32_e32 v44, v44, v45
	v_div_scale_f32 v45, s[20:21], v44, v44, 1.0
	v_rcp_f32_e32 v49, v45
	s_nop 0
	v_fma_f32 v140, -v45, v49, 1.0
	v_fmac_f32_e32 v49, v140, v49
	v_div_scale_f32 v140, vcc, 1.0, v44, 1.0
	v_mul_f32_e32 v141, v140, v49
	v_fma_f32 v142, -v45, v141, v140
	v_fmac_f32_e32 v141, v142, v49
	v_fma_f32 v45, -v45, v141, v140
	v_div_fmas_f32 v45, v45, v49, v141
	v_div_fixup_f32 v162, v45, v44, 1.0
	s_waitcnt vmcnt(15)
	ds_write_b128 v252, v[102:105]
	s_waitcnt vmcnt(14)
	ds_write_b128 v252, v[110:113] offset:1152
	s_waitcnt vmcnt(13)
	ds_write_b128 v252, v[126:129] offset:2304
	s_waitcnt vmcnt(12)
	ds_write_b128 v252, v[130:133] offset:3456
	ds_read_u16 v44, v151 offset:256
	ds_read_u16 v45, v151 offset:272
	ds_read_u16 v49, v151 offset:288
	ds_read_u16 v126, v151 offset:304
	s_waitcnt lgkmcnt(0)
	v_lshl_or_b32 v44, v44, 8, v250
	v_lshl_or_b32 v45, v45, 8, v250
	global_load_dwordx4 v[102:105], v44, s[50:51] offset:128
	global_load_dwordx4 v[110:113], v45, s[50:51] offset:128
	v_lshl_or_b32 v44, v49, 8, v250
	v_lshl_or_b32 v45, v126, 8, v250
	global_load_dwordx4 v[126:129], v44, s[50:51] offset:128
	global_load_dwordx4 v[130:133], v45, s[50:51] offset:128
	v_mul_f32_e32 v44, v162, v46
	v_mul_f32_e32 v45, v162, v47
	v_mul_f32_e32 v46, v162, v134
	v_mul_f32_e32 v47, v162, v135
	v_cvt_pk_bf16_f32 v44, v44, v45
	v_cvt_pk_bf16_f32 v45, v46, v47
	v_mul_f32_e32 v46, v162, v136
	v_mul_f32_e32 v47, v162, v137
	v_mul_f32_e32 v134, v162, v138
	v_mul_f32_e32 v135, v162, v139
	s_waitcnt lgkmcnt(0)
	v_cvt_pk_bf16_f32 v46, v46, v47
	v_cvt_pk_bf16_f32 v47, v134, v135
	ds_read_b64_tr_b16 v[136:137], v249 offset:2304
	ds_read_b64_tr_b16 v[134:135], v249
	ds_read_b64_tr_b16 v[138:139], v249 offset:32
	ds_read_b64_tr_b16 v[186:187], v249 offset:64
	ds_read_b64_tr_b16 v[190:191], v249 offset:96
	ds_read_b64_tr_b16 v[140:141], v249 offset:2336
	ds_read_b64_tr_b16 v[188:189], v249 offset:2368
	ds_read_b64_tr_b16 v[192:193], v249 offset:2400
	s_waitcnt lgkmcnt(6)
	v_mfma_f32_16x16x32_bf16 v[142:145], v[44:47], v[134:137], 0
	s_waitcnt lgkmcnt(2)
	v_mfma_f32_16x16x32_bf16 v[138:141], v[44:47], v[138:141], 0
	s_waitcnt lgkmcnt(1)
	v_mfma_f32_16x16x32_bf16 v[134:137], v[44:47], v[186:189], 0
	s_waitcnt lgkmcnt(0)
	v_mfma_f32_16x16x32_bf16 v[44:47], v[44:47], v[190:193], 0
	s_waitcnt vmcnt(15)
	ds_write_b128 v252, v[86:89] offset:4608
	s_waitcnt vmcnt(14)
	ds_write_b128 v252, v[94:97] offset:5760
	s_waitcnt vmcnt(13)
	ds_write_b128 v252, v[118:121] offset:6912
	s_waitcnt vmcnt(12)
	ds_write_b128 v252, v[122:125] offset:8064
	ds_read_u16 v49, v151 offset:320
	ds_read_u16 v86, v151 offset:336
	ds_read_u16 v118, v151 offset:352
	ds_read_u16 v119, v151 offset:368
	s_waitcnt lgkmcnt(0)
	v_lshl_or_b32 v49, v49, 8, v250
	v_lshl_or_b32 v94, v86, 8, v250
	global_load_dwordx4 v[86:89], v49, s[50:51] offset:128
	s_nop 0
	global_load_dwordx4 v[94:97], v94, s[50:51] offset:128
	v_lshl_or_b32 v49, v118, 8, v250
	v_lshl_or_b32 v122, v119, 8, v250
	global_load_dwordx4 v[118:121], v49, s[50:51] offset:128
	s_nop 0
	global_load_dwordx4 v[122:125], v122, s[50:51] offset:128
	v_mul_f32_e32 v186, v162, v226
	v_mul_f32_e32 v187, v162, v227
	v_mul_f32_e32 v188, v162, v228
	v_mul_f32_e32 v189, v162, v229
	v_cvt_pk_bf16_f32 v186, v186, v187
	v_cvt_pk_bf16_f32 v187, v188, v189
	v_mul_f32_e32 v188, v162, v230
	v_mul_f32_e32 v189, v162, v231
	v_mul_f32_e32 v190, v162, v232
	v_mul_f32_e32 v191, v162, v233
	v_cvt_pk_bf16_f32 v188, v188, v189
	v_cvt_pk_bf16_f32 v189, v190, v191
	s_waitcnt lgkmcnt(0)
	ds_read_b64_tr_b16 v[192:193], v249 offset:6912
	ds_read_b64_tr_b16 v[190:191], v249 offset:4608
	ds_read_b64_tr_b16 v[198:199], v249 offset:4640
	s_waitcnt lgkmcnt(1)
	v_mfma_f32_16x16x32_bf16 v[142:145], v[186:189], v[190:193], v[142:145]
	ds_read_b64_tr_b16 v[200:201], v249 offset:6944
	ds_read_b64_tr_b16 v[190:191], v249 offset:4672
	ds_read_b64_tr_b16 v[192:193], v249 offset:6976
	s_waitcnt lgkmcnt(0)
	v_mfma_f32_16x16x32_bf16 v[134:137], v[186:189], v[190:193], v[134:137]
	ds_read_b64_tr_b16 v[190:191], v249 offset:4704
	ds_read_b64_tr_b16 v[192:193], v249 offset:7008
	v_mfma_f32_16x16x32_bf16 v[138:141], v[186:189], v[198:201], v[138:141]
	s_waitcnt lgkmcnt(0)
	v_mfma_f32_16x16x32_bf16 v[44:47], v[186:189], v[190:193], v[44:47]
	s_waitcnt vmcnt(15)
	ds_write_b128 v252, v[78:81]
	s_waitcnt vmcnt(14)
	ds_write_b128 v252, v[82:85] offset:1152
	s_waitcnt vmcnt(13)
	ds_write_b128 v252, v[106:109] offset:2304
	s_waitcnt vmcnt(12)
	ds_write_b128 v252, v[114:117] offset:3456
	ds_read_u16 v49, v151 offset:384
	ds_read_u16 v78, v151 offset:400
	ds_read_u16 v106, v151 offset:416
	ds_read_u16 v107, v151 offset:432
	s_waitcnt lgkmcnt(0)
	v_lshl_or_b32 v49, v49, 8, v250
	v_lshl_or_b32 v82, v78, 8, v250
	global_load_dwordx4 v[78:81], v49, s[50:51] offset:128
	s_nop 0
	global_load_dwordx4 v[82:85], v82, s[50:51] offset:128
	v_lshl_or_b32 v49, v106, 8, v250
	v_lshl_or_b32 v114, v107, 8, v250
	global_load_dwordx4 v[106:109], v49, s[50:51] offset:128
	s_nop 0
	global_load_dwordx4 v[114:117], v114, s[50:51] offset:128
	v_mul_f32_e32 v186, v162, v218
	v_mul_f32_e32 v187, v162, v219
	v_mul_f32_e32 v188, v162, v220
	v_mul_f32_e32 v189, v162, v221
	v_cvt_pk_bf16_f32 v186, v186, v187
	v_cvt_pk_bf16_f32 v187, v188, v189
	v_mul_f32_e32 v188, v162, v222
	v_mul_f32_e32 v189, v162, v223
	v_mul_f32_e32 v190, v162, v224
	v_mul_f32_e32 v191, v162, v225
	v_cvt_pk_bf16_f32 v188, v188, v189
	v_cvt_pk_bf16_f32 v189, v190, v191
	s_waitcnt lgkmcnt(0)
	ds_read_b64_tr_b16 v[192:193], v249 offset:2304
	ds_read_b64_tr_b16 v[190:191], v249
	ds_read_b64_tr_b16 v[198:199], v249 offset:32
	s_waitcnt lgkmcnt(1)
	v_mfma_f32_16x16x32_bf16 v[142:145], v[186:189], v[190:193], v[142:145]
	ds_read_b64_tr_b16 v[200:201], v249 offset:2336
	ds_read_b64_tr_b16 v[190:191], v249 offset:64
	ds_read_b64_tr_b16 v[192:193], v249 offset:2368
	s_waitcnt lgkmcnt(0)
	v_mfma_f32_16x16x32_bf16 v[134:137], v[186:189], v[190:193], v[134:137]
	ds_read_b64_tr_b16 v[190:191], v249 offset:96
	ds_read_b64_tr_b16 v[192:193], v249 offset:2400
	v_mfma_f32_16x16x32_bf16 v[138:141], v[186:189], v[198:201], v[138:141]
	s_waitcnt lgkmcnt(0)
	v_mfma_f32_16x16x32_bf16 v[44:47], v[186:189], v[190:193], v[44:47]
	s_waitcnt vmcnt(15)
	ds_write_b128 v252, v[70:73] offset:4608
	s_waitcnt vmcnt(14)
	ds_write_b128 v252, v[74:77] offset:5760
	s_waitcnt vmcnt(13)
	ds_write_b128 v252, v[90:93] offset:6912
	s_waitcnt vmcnt(12)
	ds_write_b128 v252, v[98:101] offset:8064
	ds_read_u16 v49, v151 offset:448
	ds_read_u16 v70, v151 offset:464
	ds_read_u16 v90, v151 offset:480
	ds_read_u16 v91, v151 offset:496
	s_waitcnt lgkmcnt(0)
	v_lshl_or_b32 v49, v49, 8, v250
	v_lshl_or_b32 v74, v70, 8, v250
	global_load_dwordx4 v[70:73], v49, s[50:51] offset:128
	s_nop 0
	global_load_dwordx4 v[74:77], v74, s[50:51] offset:128
	v_lshl_or_b32 v49, v90, 8, v250
	v_lshl_or_b32 v98, v91, 8, v250
	global_load_dwordx4 v[90:93], v49, s[50:51] offset:128
	s_nop 0
	global_load_dwordx4 v[98:101], v98, s[50:51] offset:128
	v_mul_f32_e32 v186, v162, v206
	v_mul_f32_e32 v187, v162, v207
	v_mul_f32_e32 v188, v162, v208
	v_mul_f32_e32 v189, v162, v209
	v_cvt_pk_bf16_f32 v186, v186, v187
	v_cvt_pk_bf16_f32 v187, v188, v189
	v_mul_f32_e32 v188, v162, v214
	v_mul_f32_e32 v189, v162, v215
	v_mul_f32_e32 v190, v162, v216
	v_mul_f32_e32 v191, v162, v217
	v_cvt_pk_bf16_f32 v188, v188, v189
	v_cvt_pk_bf16_f32 v189, v190, v191
	s_waitcnt lgkmcnt(0)
	ds_read_b64_tr_b16 v[192:193], v249 offset:6912
	ds_read_b64_tr_b16 v[190:191], v249 offset:4608
	ds_read_b64_tr_b16 v[198:199], v249 offset:4640
	s_waitcnt lgkmcnt(1)
	v_mfma_f32_16x16x32_bf16 v[142:145], v[186:189], v[190:193], v[142:145]
	ds_read_b64_tr_b16 v[200:201], v249 offset:6944
	ds_read_b64_tr_b16 v[190:191], v249 offset:4672
	ds_read_b64_tr_b16 v[192:193], v249 offset:6976
	s_waitcnt lgkmcnt(0)
	v_mfma_f32_16x16x32_bf16 v[134:137], v[186:189], v[190:193], v[134:137]
	ds_read_b64_tr_b16 v[190:191], v249 offset:4704
	ds_read_b64_tr_b16 v[192:193], v249 offset:7008
	v_mfma_f32_16x16x32_bf16 v[138:141], v[186:189], v[198:201], v[138:141]
	s_waitcnt lgkmcnt(0)
	v_mfma_f32_16x16x32_bf16 v[44:47], v[186:189], v[190:193], v[44:47]
	v_mul_f32_e32 v182, v162, v182
	v_mul_f32_e32 v183, v162, v183
	v_mul_f32_e32 v180, v162, v180
	v_mul_f32_e32 v181, v162, v181
	v_cvt_pk_bf16_f32 v182, v182, v183
	v_cvt_pk_bf16_f32 v183, v180, v181
	v_mul_f32_e32 v180, v162, v184
	v_mul_f32_e32 v181, v162, v185
	s_waitcnt vmcnt(15)
	ds_write_b128 v252, v[102:105]
	s_waitcnt vmcnt(14)
	ds_write_b128 v252, v[110:113] offset:1152
	s_waitcnt vmcnt(13)
	ds_write_b128 v252, v[126:129] offset:2304
	s_waitcnt vmcnt(12)
	ds_write_b128 v252, v[130:133] offset:3456
	v_cvt_pk_bf16_f32 v184, v180, v181
	v_mul_f32_e32 v180, v162, v196
	v_mul_f32_e32 v181, v162, v197
	v_cvt_pk_bf16_f32 v185, v180, v181
	s_waitcnt lgkmcnt(0)
	ds_read_b64_tr_b16 v[188:189], v249 offset:2304
	ds_read_b64_tr_b16 v[186:187], v249
	ds_read_b64_tr_b16 v[190:191], v249 offset:32
	s_waitcnt lgkmcnt(1)
	v_mfma_f32_16x16x32_bf16 v[142:145], v[182:185], v[186:189], v[142:145]
	ds_read_b64_tr_b16 v[192:193], v249 offset:2336
	ds_read_b64_tr_b16 v[186:187], v249 offset:64
	ds_read_b64_tr_b16 v[188:189], v249 offset:2368
	s_waitcnt lgkmcnt(0)
	v_mfma_f32_16x16x32_bf16 v[134:137], v[182:185], v[186:189], v[134:137]
	ds_read_b64_tr_b16 v[186:187], v249 offset:96
	ds_read_b64_tr_b16 v[188:189], v249 offset:2400
	v_mfma_f32_16x16x32_bf16 v[138:141], v[182:185], v[190:193], v[138:141]
	s_waitcnt lgkmcnt(0)
	v_mfma_f32_16x16x32_bf16 v[44:47], v[182:185], v[186:189], v[44:47]
	v_mul_f32_e32 v172, v162, v172
	v_mul_f32_e32 v173, v162, v173
	v_mul_f32_e32 v174, v162, v174
	v_mul_f32_e32 v175, v162, v175
	s_waitcnt vmcnt(11)
	ds_write_b128 v252, v[86:89] offset:4608
	s_waitcnt vmcnt(10)
	ds_write_b128 v252, v[94:97] offset:5760
	s_waitcnt vmcnt(9)
	ds_write_b128 v252, v[118:121] offset:6912
	s_waitcnt vmcnt(8)
	ds_write_b128 v252, v[122:125] offset:8064
	v_cvt_pk_bf16_f32 v172, v172, v173
	v_cvt_pk_bf16_f32 v173, v174, v175
	v_mul_f32_e32 v174, v162, v176
	v_mul_f32_e32 v175, v162, v177
	v_mul_f32_e32 v176, v162, v178
	v_mul_f32_e32 v177, v162, v179
	v_cvt_pk_bf16_f32 v174, v174, v175
	v_cvt_pk_bf16_f32 v175, v176, v177
	s_waitcnt lgkmcnt(0)
	ds_read_b64_tr_b16 v[178:179], v249 offset:6912
	ds_read_b64_tr_b16 v[176:177], v249 offset:4608
	ds_read_b64_tr_b16 v[180:181], v249 offset:4640
	s_waitcnt lgkmcnt(1)
	v_mfma_f32_16x16x32_bf16 v[142:145], v[172:175], v[176:179], v[142:145]
	ds_read_b64_tr_b16 v[182:183], v249 offset:6944
	ds_read_b64_tr_b16 v[176:177], v249 offset:4672
	ds_read_b64_tr_b16 v[178:179], v249 offset:6976
	s_waitcnt lgkmcnt(0)
	v_mfma_f32_16x16x32_bf16 v[134:137], v[172:175], v[176:179], v[134:137]
	ds_read_b64_tr_b16 v[176:177], v249 offset:4704
	ds_read_b64_tr_b16 v[178:179], v249 offset:7008
	v_mfma_f32_16x16x32_bf16 v[138:141], v[172:175], v[180:183], v[138:141]
	s_waitcnt lgkmcnt(0)
	v_mfma_f32_16x16x32_bf16 v[44:47], v[172:175], v[176:179], v[44:47]
	v_mul_f32_e32 v164, v162, v164
	v_mul_f32_e32 v165, v162, v165
	v_mul_f32_e32 v166, v162, v166
	v_mul_f32_e32 v167, v162, v167
	s_waitcnt vmcnt(7)
	ds_write_b128 v252, v[78:81]
	s_waitcnt vmcnt(6)
	ds_write_b128 v252, v[82:85] offset:1152
	s_waitcnt vmcnt(5)
	ds_write_b128 v252, v[106:109] offset:2304
	s_waitcnt vmcnt(4)
	ds_write_b128 v252, v[114:117] offset:3456
	v_cvt_pk_bf16_f32 v164, v164, v165
	v_cvt_pk_bf16_f32 v165, v166, v167
	v_mul_f32_e32 v166, v162, v168
	v_mul_f32_e32 v167, v162, v169
	v_mul_f32_e32 v168, v162, v170
	v_mul_f32_e32 v169, v162, v171
	v_cvt_pk_bf16_f32 v166, v166, v167
	v_cvt_pk_bf16_f32 v167, v168, v169
	s_waitcnt lgkmcnt(0)
	ds_read_b64_tr_b16 v[170:171], v249 offset:2304
	ds_read_b64_tr_b16 v[168:169], v249
	ds_read_b64_tr_b16 v[172:173], v249 offset:32
	s_waitcnt lgkmcnt(1)
	v_mfma_f32_16x16x32_bf16 v[142:145], v[164:167], v[168:171], v[142:145]
	ds_read_b64_tr_b16 v[174:175], v249 offset:2336
	ds_read_b64_tr_b16 v[168:169], v249 offset:64
	ds_read_b64_tr_b16 v[170:171], v249 offset:2368
	s_waitcnt lgkmcnt(0)
	v_mfma_f32_16x16x32_bf16 v[134:137], v[164:167], v[168:171], v[134:137]
	ds_read_b64_tr_b16 v[168:169], v249 offset:96
	ds_read_b64_tr_b16 v[170:171], v249 offset:2400
	v_mfma_f32_16x16x32_bf16 v[138:141], v[164:167], v[172:175], v[138:141]
	s_waitcnt lgkmcnt(0)
	v_mfma_f32_16x16x32_bf16 v[44:47], v[164:167], v[168:171], v[44:47]
	v_mul_f32_e32 v154, v162, v154
	v_mul_f32_e32 v155, v162, v155
	v_mul_f32_e32 v156, v162, v156
	v_mul_f32_e32 v157, v162, v157
	s_waitcnt vmcnt(3)
	ds_write_b128 v252, v[70:73] offset:4608
	s_waitcnt vmcnt(2)
	ds_write_b128 v252, v[74:77] offset:5760
	s_waitcnt vmcnt(1)
	ds_write_b128 v252, v[90:93] offset:6912
	s_waitcnt vmcnt(0)
	ds_write_b128 v252, v[98:101] offset:8064
	v_cvt_pk_bf16_f32 v154, v154, v155
	v_cvt_pk_bf16_f32 v155, v156, v157
	v_mul_f32_e32 v156, v162, v158
	v_mul_f32_e32 v157, v162, v159
	v_mul_f32_e32 v158, v162, v160
	v_mul_f32_e32 v159, v162, v161
	v_cvt_pk_bf16_f32 v156, v156, v157
	v_cvt_pk_bf16_f32 v157, v158, v159
	s_waitcnt lgkmcnt(0)
	ds_read_b64_tr_b16 v[160:161], v249 offset:6912
	ds_read_b64_tr_b16 v[158:159], v249 offset:4608
	ds_read_b64_tr_b16 v[162:163], v249 offset:4640
	s_waitcnt lgkmcnt(1)
	v_mfma_f32_16x16x32_bf16 v[142:145], v[154:157], v[158:161], v[142:145]
	ds_read_b64_tr_b16 v[164:165], v249 offset:6944
	ds_read_b64_tr_b16 v[158:159], v249 offset:4672
	ds_read_b64_tr_b16 v[160:161], v249 offset:6976
	s_waitcnt lgkmcnt(0)
	v_mfma_f32_16x16x32_bf16 v[134:137], v[154:157], v[158:161], v[134:137]
	ds_read_b64_tr_b16 v[158:159], v249 offset:4704
	ds_read_b64_tr_b16 v[160:161], v249 offset:7008
	v_mfma_f32_16x16x32_bf16 v[138:141], v[154:157], v[162:165], v[138:141]
	s_waitcnt lgkmcnt(0)
	v_mfma_f32_16x16x32_bf16 v[44:47], v[154:157], v[158:161], v[44:47]
	s_waitcnt lgkmcnt(0)
	s_and_saveexec_b64 s[8:9], s[40:41]
	s_cbranch_execz .LBB0_784
	s_lshl_b64 s[18:19], s[52:53], 10
	v_lshl_add_u64 v[154:155], v[148:149], 0, s[18:19]
	v_cvt_pk_bf16_f32 v49, v142, v143
	global_store_short v[154:155], v49, off
	global_store_short_d16_hi v[154:155], v49, off offset:128
	v_cvt_pk_bf16_f32 v49, v144, v145
	global_store_short v[154:155], v49, off offset:256
	global_store_short_d16_hi v[154:155], v49, off offset:384
	v_cvt_pk_bf16_f32 v49, v138, v139
	global_store_short v[154:155], v49, off offset:32
	global_store_short_d16_hi v[154:155], v49, off offset:160
	v_cvt_pk_bf16_f32 v49, v140, v141
	global_store_short v[154:155], v49, off offset:288
	global_store_short_d16_hi v[154:155], v49, off offset:416
	v_cvt_pk_bf16_f32 v49, v134, v135
	global_store_short v[154:155], v49, off offset:64
	global_store_short_d16_hi v[154:155], v49, off offset:192
	v_cvt_pk_bf16_f32 v49, v136, v137
	global_store_short v[154:155], v49, off offset:320
	global_store_short_d16_hi v[154:155], v49, off offset:448
	v_cvt_pk_bf16_f32 v49, v44, v45
	global_store_short v[154:155], v49, off offset:96
	global_store_short_d16_hi v[154:155], v49, off offset:224
	v_cvt_pk_bf16_f32 v49, v46, v47
	global_store_short v[154:155], v49, off offset:352
	global_store_short_d16_hi v[154:155], v49, off offset:480
	s_branch .LBB0_784
